# LN1 row loop: next-row prefetch issued at the top of the iteration (no loads left in the body), body waits relaxed to vmcnt(3)
# speedup vs baseline: 1.0131x; 1.0014x over previous
; #define GAS __attribute__((address_space(1)))
; __device__ __forceinline__ void unpack8(const u32x4 q, float* o) { o[0] = bflo(q.x); o[1] = bfhi(q.x); o[2] = bflo(q.y); o[3] = bfhi(q.y); o[4] = bflo(q.z); o[5] = bfhi(q.z); o[6] = bflo(q.w); o[7] = bfhi(q.w); }
; __device__ __forceinline__ const float* mod_ptr(const Frame& F, int l, int row) { return (const float*)(F.ws + WS_MOD) + ((size_t)l * 17 + row_b(row)) * 6144; }
; __device__ __forceinline__ void ph_ln1(Frame& F, int l, int ntok) {
;     ...
;     for (int row = gw; row < ntok; row += NGW) {
;         bf16_t* xr = (bf16_t*)(F.ws + WS_XR) + (size_t)row * DM;
;         const unsigned char* yr = (const unsigned char*)(F.ws + WS_Y) + (size_t)row * DM + 16 * F.lane;
;         const float* md = mod_ptr(F, l, row);
;         const u32x4 xa = __builtin_nontemporal_load((const GAS u32x4*)(xr + cA)), xb = __builtin_nontemporal_load((const GAS u32x4*)(xr + cA + 128)), ya = __builtin_nontemporal_load((const GAS u32x4*)yr);
;         float x[16], y[16], v[16]; unpack8(xa, x); unpack8(xb, x + 8);
;         { const unsigned a[4] = {ya.x, ya.y, ya.z, ya.w};
; #pragma unroll
;           for (int e = 0; e < 4; ++e) { const f32x2 lo = __builtin_amdgcn_cvt_pk_f32_fp8((int)a[e], false), hi = __builtin_amdgcn_cvt_pk_f32_fp8((int)a[e], true); y[4 * e] = lo.x; y[4 * e + 1] = lo.y; y[4 * e + 2] = hi.x; y[4 * e + 3] = hi.y; } }
;         float s = 0.f;
; #pragma unroll
;         for (int j = 0; j < 4; ++j) { const f32x4 g1 = *(const GAS f32x4*)(md + 2048 + LN1_COL(j));
; #pragma unroll
;             for (int e = 0; e < 4; ++e) { v[4 * j + e] = x[4 * j + e] * DN_ALPHA + g1[e] * y[4 * j + e]; s += v[4 * j + e]; } }
;         const float mean = wave_sum(s, F.lane) * (1.f / DM); float s2 = 0.f;
; #pragma unroll
;         for (int e = 0; e < 16; ++e) { v[e] -= mean; s2 += v[e] * v[e]; }
;         const float rstd = 1.f / sqrtf(wave_sum(s2, F.lane) * (1.f / DM) + LN_EPS);
;         unsigned wx[8]; int w8[4];
; #pragma unroll
;         for (int j = 0; j < 4; ++j) { const f32x4 g = *(const GAS f32x4*)(lg + LN1_COL(j)), bb = *(const GAS f32x4*)(lb + LN1_COL(j)), sh = *(const GAS f32x4*)(md + 3072 + LN1_COL(j)), sc = *(const GAS f32x4*)(md + 4096 + LN1_COL(j));
.Lln1_md_keep:
	s_waitcnt vmcnt(0)
	v_mov_b32_e32 v46, v128
	v_mov_b32_e32 v47, v129
	v_mov_b32_e32 v48, v130
	v_mov_b32_e32 v49, v131
	v_mov_b32_e32 v90, v132
	v_mov_b32_e32 v91, v133
	v_mov_b32_e32 v92, v134
	v_mov_b32_e32 v93, v135
	v_mov_b32_e32 v0, v144
	v_mov_b32_e32 v1, v145
	v_mov_b32_e32 v2, v146
	v_mov_b32_e32 v3, v147
	s_add_i32 s87, s40, s8
	s_cmp_lt_i32 s87, s80
	s_cselect_b64 s[86:87], -1, 0
	v_lshl_add_u64 v[148:149], s[38:39], 0, v[62:63]
	v_lshl_add_u64 v[148:149], v[148:149], 0, s[84:85]
	v_lshl_add_u64 v[150:151], s[38:39], 0, v[64:65]
	v_cndmask_b32_e64 v148, v68, v148, s[86:87]
	v_cndmask_b32_e64 v149, v69, v149, s[86:87]
	v_cndmask_b32_e64 v150, v68, v150, s[86:87]
	v_cndmask_b32_e64 v151, v69, v151, s[86:87]
	global_load_dwordx4 v[128:131], v[148:149], off nt
	global_load_dwordx4 v[132:135], v[148:149], off offset:256 nt
	global_load_dwordx4 v[144:147], v[150:151], off nt
	v_lshlrev_b32_e32 v122, 16, v93
	v_cvt_pk_f32_fp8_e32 v[24:25], v0
	v_cvt_pk_f32_fp8_sdwa v[70:71], v0 src0_sel:WORD_1
	v_cvt_pk_f32_fp8_e32 v[72:73], v1
	v_cvt_pk_f32_fp8_sdwa v[74:75], v1 src0_sel:WORD_1
	v_lshl_add_u64 v[0:1], s[2:3], 0, v[54:55]
	v_mov_b32_e32 v50, v136
	v_mov_b32_e32 v51, v137
	v_mov_b32_e32 v52, v138
	v_mov_b32_e32 v53, v139
	v_mov_b32_e32 v94, v140
	v_mov_b32_e32 v95, v141
	v_mov_b32_e32 v96, v142
	v_mov_b32_e32 v97, v143
	v_lshl_add_u64 v[0:1], s[2:3], 0, v[66:67]
	v_mov_b32_e32 v98, v152
	v_mov_b32_e32 v99, v153
	v_mov_b32_e32 v100, v154
	v_mov_b32_e32 v101, v155
	v_mov_b32_e32 v102, v188
	v_mov_b32_e32 v103, v189
	v_mov_b32_e32 v104, v190
	v_mov_b32_e32 v105, v191
	s_add_u32 s2, s0, 0x4000
	s_addc_u32 s3, s4, 0
	v_lshl_add_u64 v[0:1], s[36:37], 0, v[54:55]
	v_lshl_add_u64 v[4:5], s[2:3], 0, v[54:55]
	v_cvt_pk_f32_fp8_e32 v[114:115], v2
	v_cvt_pk_f32_fp8_sdwa v[116:117], v2 src0_sel:WORD_1
	v_cvt_pk_f32_fp8_e32 v[118:119], v3
	v_cvt_pk_f32_fp8_sdwa v[120:121], v3 src0_sel:WORD_1
	v_mov_b32_e32 v26, v156
	v_mov_b32_e32 v27, v157
	v_mov_b32_e32 v28, v158
	v_mov_b32_e32 v29, v159
	v_mov_b32_e32 v106, v160
	v_mov_b32_e32 v107, v161
	v_mov_b32_e32 v108, v162
	v_mov_b32_e32 v109, v163
	v_mov_b32_e32 v30, v164
	v_mov_b32_e32 v31, v165
	v_mov_b32_e32 v32, v166
	v_mov_b32_e32 v33, v167
	v_mov_b32_e32 v110, v168
	v_mov_b32_e32 v111, v169
	v_mov_b32_e32 v112, v170
	v_mov_b32_e32 v113, v171
	v_mov_b32_e32 v12, v194
	v_mov_b32_e32 v13, v195
	v_mov_b32_e32 v14, v196
	v_mov_b32_e32 v15, v197
	v_mov_b32_e32 v42, v198
	v_mov_b32_e32 v43, v199
	v_mov_b32_e32 v44, v200
	v_mov_b32_e32 v45, v201
	s_nop 0
	v_mov_b32_e32 v0, v202
	v_mov_b32_e32 v1, v203
	v_mov_b32_e32 v2, v204
	v_mov_b32_e32 v3, v205
	s_nop 0
	v_mov_b32_e32 v4, v206
	v_mov_b32_e32 v5, v207
	v_mov_b32_e32 v6, v208
	v_mov_b32_e32 v7, v209
	v_and_b32_e32 v123, 0xffff0000, v93
	v_lshl_add_u64 v[82:83], s[2:3], 0, v[66:67]
	s_waitcnt lgkmcnt(0)
	v_mov_b32_e32 v8, v172
	v_mov_b32_e32 v9, v173
	v_mov_b32_e32 v10, v174
	v_mov_b32_e32 v11, v175
	v_mov_b32_e32 v34, v176
	v_mov_b32_e32 v35, v177
	v_mov_b32_e32 v36, v178
	v_mov_b32_e32 v37, v179
	v_mov_b32_e32 v16, v180
	v_mov_b32_e32 v17, v181
	v_mov_b32_e32 v18, v182
	v_mov_b32_e32 v19, v183
	v_mov_b32_e32 v38, v184
	v_mov_b32_e32 v39, v185
	v_mov_b32_e32 v40, v186
	v_mov_b32_e32 v41, v187
	s_mov_b32 s0, 0x5be00000
	s_add_i32 s40, s40, s8
	s_cmp_lt_i32 s40, s80
	s_waitcnt vmcnt(3)
	v_pk_mul_f32 v[52:53], v[70:71], v[52:53]
	v_lshlrev_b32_e32 v70, 16, v46
	v_and_b32_e32 v71, 0xffff0000, v46
	v_pk_mul_f32 v[24:25], v[24:25], v[50:51]
	s_waitcnt vmcnt(3)
	v_pk_mul_f32 v[104:105], v[120:121], v[104:105]
	v_lshlrev_b32_e32 v120, 16, v92
	v_and_b32_e32 v121, 0xffff0000, v92
	v_pk_mul_f32 v[92:93], v[118:119], v[102:103]
	v_lshlrev_b32_e32 v102, 16, v91
	v_and_b32_e32 v103, 0xffff0000, v91
	v_pk_mul_f32 v[100:101], v[116:117], v[100:101]
	v_pk_fma_f32 v[24:25], v[70:71], s[20:21], v[24:25] op_sel_hi:[1,0,1]
	v_pk_fma_f32 v[100:101], v[102:103], s[20:21], v[100:101] op_sel_hi:[1,0,1]
	v_lshlrev_b32_e32 v102, 16, v90
	v_and_b32_e32 v103, 0xffff0000, v90
	v_pk_mul_f32 v[90:91], v[114:115], v[98:99]
	v_lshlrev_b32_e32 v98, 16, v49
	v_and_b32_e32 v99, 0xffff0000, v49
	v_pk_mul_f32 v[74:75], v[74:75], v[96:97]
	v_lshlrev_b32_e32 v96, 16, v48
	v_and_b32_e32 v97, 0xffff0000, v48
	v_pk_mul_f32 v[48:49], v[72:73], v[94:95]
	v_lshlrev_b32_e32 v72, 16, v47
	v_and_b32_e32 v73, 0xffff0000, v47
	v_add_f32_e32 v46, 0, v24
	v_pk_fma_f32 v[52:53], v[72:73], s[20:21], v[52:53] op_sel_hi:[1,0,1]
	v_add_f32_e32 v46, v25, v46
	v_add_f32_e32 v46, v52, v46
	v_pk_fma_f32 v[48:49], v[96:97], s[20:21], v[48:49] op_sel_hi:[1,0,1]
	v_add_f32_e32 v46, v53, v46
	v_add_f32_e32 v46, v48, v46
	v_pk_fma_f32 v[74:75], v[98:99], s[20:21], v[74:75] op_sel_hi:[1,0,1]
	v_add_f32_e32 v46, v49, v46
	v_add_f32_e32 v46, v74, v46
	v_pk_fma_f32 v[90:91], v[102:103], s[20:21], v[90:91] op_sel_hi:[1,0,1]
	v_add_f32_e32 v46, v75, v46
	v_add_f32_e32 v46, v90, v46
	v_add_f32_e32 v46, v91, v46
	v_add_f32_e32 v46, v100, v46
	v_pk_fma_f32 v[92:93], v[120:121], s[20:21], v[92:93] op_sel_hi:[1,0,1]
	v_add_f32_e32 v46, v101, v46
	v_add_f32_e32 v46, v92, v46
	v_pk_fma_f32 v[104:105], v[122:123], s[20:21], v[104:105] op_sel_hi:[1,0,1]
	v_add_f32_e32 v46, v93, v46
	v_add_f32_e32 v46, v104, v46
	v_add_f32_e32 v46, v105, v46
	ds_bpermute_b32 v47, v76, v46
	s_waitcnt vmcnt(3)
	v_add_f32_e32 v124, 1.0, v4
	v_add_f32_e32 v125, 1.0, v5
	v_lshl_add_u64 v[4:5], s[36:37], 0, v[66:67]
	v_add_f32_e32 v126, 1.0, v6
	s_waitcnt lgkmcnt(0)
	v_add_f32_e32 v46, v46, v47
	ds_bpermute_b32 v47, v77, v46
	v_add_f32_e32 v127, 1.0, v7
	v_add_f32_e32 v86, 1.0, v0
	v_add_f32_e32 v87, 1.0, v1
	v_add_f32_e32 v88, 1.0, v2
	s_waitcnt lgkmcnt(0)
; #define GAS __attribute__((address_space(1)))
; __device__ __forceinline__ unsigned pk2(float lo, float hi) { const f32x2 v = {lo, hi}; const bf16v2 b = __builtin_convertvector(v, bf16v2); return __builtin_bit_cast(unsigned, b); }
; __device__ __forceinline__ void ph_ln1(Frame& F, int l, int ntok) {
;     ...
;         const float mean = wave_sum(s, F.lane) * (1.f / DM); float s2 = 0.f;
; #pragma unroll
;         for (int e = 0; e < 16; ++e) { v[e] -= mean; s2 += v[e] * v[e]; }
;         const float rstd = 1.f / sqrtf(wave_sum(s2, F.lane) * (1.f / DM) + LN_EPS);
;         unsigned wx[8]; int w8[4];
; #pragma unroll
;         for (int j = 0; j < 4; ++j) { const f32x4 g = *(const GAS f32x4*)(lg + LN1_COL(j)), bb = *(const GAS f32x4*)(lb + LN1_COL(j)), sh = *(const GAS f32x4*)(md + 3072 + LN1_COL(j)), sc = *(const GAS f32x4*)(md + 4096 + LN1_COL(j));
;             float xn[4];
; #pragma unroll
;             for (int e = 0; e < 4; ++e) xn[e] = v[4 * j + e] * rstd * g[e] + bb[e];
;             wx[2 * j] = pk2(xn[0], xn[1]); wx[2 * j + 1] = pk2(xn[2], xn[3]);
;             const float h0 = xn[0] * (1.f + sc[0]) + sh[0], h1 = xn[1] * (1.f + sc[1]) + sh[1], h2 = xn[2] * (1.f + sc[2]) + sh[2], h3 = xn[3] * (1.f + sc[3]) + sh[3];
;             int v = 0; v = __builtin_amdgcn_cvt_pk_fp8_f32(h0, h1, v, false); v = __builtin_amdgcn_cvt_pk_fp8_f32(h2, h3, v, true); w8[j] = v; }
;         unsigned char* x8 = (unsigned char*)(F.ws + WS_XM8) + (size_t)row * DM;
;         __builtin_nontemporal_store((u32x2){(unsigned)w8[0], (unsigned)w8[1]}, (GAS u32x2*)(x8 + cA)); __builtin_nontemporal_store((u32x2){(unsigned)w8[2], (unsigned)w8[3]}, (GAS u32x2*)(x8 + cA + 128));
;         __builtin_nontemporal_store((u32x4){wx[0], wx[1], wx[2], wx[3]}, (GAS u32x4*)(xr + cA)); __builtin_nontemporal_store((u32x4){wx[4], wx[5], wx[6], wx[7]}, (GAS u32x4*)(xr + cA + 128));
	v_add_f32_e32 v46, v46, v47
	ds_bpermute_b32 v47, v78, v46
	v_add_f32_e32 v89, 1.0, v3
	v_mov_b32_e32 v0, v210
	v_mov_b32_e32 v1, v211
	v_mov_b32_e32 v2, v212
	v_mov_b32_e32 v3, v213
	v_mov_b32_e32 v20, v214
	v_mov_b32_e32 v21, v215
	v_mov_b32_e32 v22, v216
	v_mov_b32_e32 v23, v217
	s_nop 0
	v_mov_b32_e32 v4, v218
	v_mov_b32_e32 v5, v219
	v_mov_b32_e32 v6, v220
	v_mov_b32_e32 v7, v221
	s_nop 0
	v_mov_b32_e32 v82, v222
	v_mov_b32_e32 v83, v223
	v_mov_b32_e32 v84, v224
	v_mov_b32_e32 v85, v225
	s_waitcnt lgkmcnt(0)
	v_add_f32_e32 v46, v46, v47
	ds_bpermute_b32 v47, v79, v46
	s_waitcnt lgkmcnt(0)
	v_add_f32_e32 v46, v46, v47
	ds_bpermute_b32 v47, v80, v46
	s_waitcnt lgkmcnt(0)
	v_add_f32_e32 v46, v46, v47
	ds_bpermute_b32 v47, v81, v46
	s_waitcnt lgkmcnt(0)
	v_add_f32_e32 v46, v46, v47
	v_mul_f32_e32 v50, 0x3a800000, v46
	v_pk_add_f32 v[24:25], v[24:25], v[50:51] op_sel_hi:[1,0] neg_lo:[0,1] neg_hi:[0,1]
	v_pk_add_f32 v[96:97], v[52:53], v[50:51] op_sel_hi:[1,0] neg_lo:[0,1] neg_hi:[0,1]
	v_pk_mul_f32 v[94:95], v[24:25], v[24:25]
	v_pk_mul_f32 v[98:99], v[96:97], v[96:97]
	v_add_f32_e32 v94, v94, v95
	v_pk_add_f32 v[72:73], v[48:49], v[50:51] op_sel_hi:[1,0] neg_lo:[0,1] neg_hi:[0,1]
	v_add_f32_e32 v94, v98, v94
	v_pk_mul_f32 v[102:103], v[72:73], v[72:73]
	v_add_f32_e32 v94, v99, v94
	v_pk_add_f32 v[74:75], v[74:75], v[50:51] op_sel_hi:[1,0] neg_lo:[0,1] neg_hi:[0,1]
	v_add_f32_e32 v94, v102, v94
	v_pk_mul_f32 v[114:115], v[74:75], v[74:75]
	v_add_f32_e32 v94, v103, v94
	v_pk_add_f32 v[52:53], v[90:91], v[50:51] op_sel_hi:[1,0] neg_lo:[0,1] neg_hi:[0,1]
	v_add_f32_e32 v94, v114, v94
	v_pk_mul_f32 v[90:91], v[52:53], v[52:53]
	v_add_f32_e32 v94, v115, v94
	v_pk_add_f32 v[70:71], v[100:101], v[50:51] op_sel_hi:[1,0] neg_lo:[0,1] neg_hi:[0,1]
	v_add_f32_e32 v90, v90, v94
	v_pk_mul_f32 v[100:101], v[70:71], v[70:71]
	v_add_f32_e32 v90, v91, v90
	v_pk_add_f32 v[46:47], v[92:93], v[50:51] op_sel_hi:[1,0] neg_lo:[0,1] neg_hi:[0,1]
	v_add_f32_e32 v90, v100, v90
	v_pk_mul_f32 v[92:93], v[46:47], v[46:47]
	v_add_f32_e32 v90, v101, v90
	v_pk_add_f32 v[48:49], v[104:105], v[50:51] op_sel_hi:[1,0] neg_lo:[0,1] neg_hi:[0,1]
	v_add_f32_e32 v90, v92, v90
	v_pk_mul_f32 v[50:51], v[48:49], v[48:49]
	v_add_f32_e32 v90, v93, v90
	v_add_f32_e32 v50, v50, v90
	v_add_f32_e32 v50, v51, v50
	ds_bpermute_b32 v51, v76, v50
	s_waitcnt lgkmcnt(0)
	v_add_f32_e32 v50, v50, v51
	ds_bpermute_b32 v51, v77, v50
	s_waitcnt lgkmcnt(0)
	v_add_f32_e32 v50, v50, v51
	ds_bpermute_b32 v51, v78, v50
	s_waitcnt lgkmcnt(0)
	v_add_f32_e32 v50, v50, v51
	ds_bpermute_b32 v51, v79, v50
	s_waitcnt lgkmcnt(0)
	v_add_f32_e32 v50, v50, v51
	ds_bpermute_b32 v51, v80, v50
	s_waitcnt vmcnt(3)
	v_add_f32_e32 v4, 1.0, v4
	s_waitcnt vmcnt(3)
	v_add_f32_e32 v82, 1.0, v82
	v_add_f32_e32 v83, 1.0, v83
	s_waitcnt lgkmcnt(0)
	v_add_f32_e32 v50, v50, v51
	ds_bpermute_b32 v51, v81, v50
	v_add_f32_e32 v84, 1.0, v84
	v_add_f32_e32 v85, 1.0, v85
	s_waitcnt lgkmcnt(0)
	v_add_f32_e32 v50, v50, v51
	v_fmamk_f32 v50, v50, 0x3a800000, v234
	v_cmp_gt_f32_e32 vcc, s9, v50
	v_mul_f32_e32 v51, 0x4f800000, v50
	s_nop 0
	v_cndmask_b32_e32 v50, v50, v51, vcc
	v_sqrt_f32_e32 v51, v50
	s_nop 0
	v_add_u32_e32 v90, -1, v51
	v_fma_f32 v91, -v90, v51, v50
	v_cmp_ge_f32_e64 s[36:37], 0, v91
	v_add_u32_e32 v91, 1, v51
	s_nop 0
	v_cndmask_b32_e64 v90, v51, v90, s[36:37]
	v_fma_f32 v51, -v91, v51, v50
	v_cmp_lt_f32_e64 s[36:37], 0, v51
	s_nop 1
	v_cndmask_b32_e64 v51, v90, v91, s[36:37]
	v_mul_f32_e32 v90, 0x37800000, v51
	v_cndmask_b32_e32 v51, v51, v90, vcc
	v_cmp_class_f32_e32 vcc, v50, v232
	s_nop 1
	v_cndmask_b32_e32 v50, v51, v50, vcc
	v_div_scale_f32 v51, s[2:3], v50, v50, 1.0
	v_rcp_f32_e32 v90, v51
	s_nop 0
	v_fma_f32 v91, -v51, v90, 1.0
	v_fmac_f32_e32 v90, v91, v90
	v_div_scale_f32 v91, vcc, 1.0, v50, 1.0
	v_mul_f32_e32 v92, v91, v90
	v_fma_f32 v93, -v51, v92, v91
	v_fmac_f32_e32 v92, v93, v90
	v_fma_f32 v51, -v51, v92, v91
	v_div_fmas_f32 v51, v51, v90, v92
	v_div_fixup_f32 v50, v51, v50, 1.0
	v_pk_mul_f32 v[24:25], v[24:25], v[50:51] op_sel_hi:[1,0]
	s_nop 0
	v_pk_fma_f32 v[90:91], v[106:107], v[24:25], v[110:111]
	v_pk_mul_f32 v[24:25], v[96:97], v[50:51] op_sel_hi:[1,0]
	v_fma_f32 v42, v124, v90, v42
	v_pk_fma_f32 v[92:93], v[108:109], v[24:25], v[112:113]
	v_cvt_pk_bf16_f32 v24, v90, v91
	v_fma_f32 v43, v125, v91, v43
	v_mov_b32_e32 v90, v193
	v_cvt_pk_fp8_f32 v90, v42, v43
	v_pk_mul_f32 v[42:43], v[72:73], v[50:51] op_sel_hi:[1,0]
	v_mov_b32_e32 v91, v193
	v_pk_fma_f32 v[30:31], v[26:27], v[42:43], v[30:31]
	v_pk_mul_f32 v[26:27], v[74:75], v[50:51] op_sel_hi:[1,0]
	v_fma_f32 v12, v86, v30, v12
	v_fma_f32 v13, v87, v31, v13
	v_cvt_pk_fp8_f32 v91, v12, v13
	v_pk_fma_f32 v[28:29], v[28:29], v[26:27], v[32:33]
	v_pk_mul_f32 v[12:13], v[52:53], v[50:51] op_sel_hi:[1,0]
	v_fma_f32 v14, v88, v28, v14
	v_fmac_f32_e32 v15, v89, v29
	v_cvt_pk_fp8_f32 v91, v14, v15 op_sel:[0,0,1]
	v_pk_fma_f32 v[14:15], v[34:35], v[12:13], v[38:39]
	v_pk_mul_f32 v[12:13], v[70:71], v[50:51] op_sel_hi:[1,0]
	v_cvt_pk_bf16_f32 v27, v28, v29
	v_pk_fma_f32 v[28:29], v[36:37], v[12:13], v[40:41]
	v_cvt_pk_bf16_f32 v12, v14, v15
	v_fma_f32 v14, v82, v14, v20
	v_fma_f32 v15, v83, v15, v21
	v_mov_b32_e32 v20, v193
	v_cvt_pk_fp8_f32 v20, v14, v15
	v_pk_mul_f32 v[14:15], v[46:47], v[50:51] op_sel_hi:[1,0]
	v_fma_f32 v21, v84, v28, v22
	v_pk_fma_f32 v[8:9], v[8:9], v[14:15], v[16:17]
	v_fmac_f32_e32 v23, v85, v29
	v_fma_f32 v0, v4, v8, v0
	v_add_f32_e32 v4, 1.0, v5
	v_cvt_pk_fp8_f32 v20, v21, v23 op_sel:[0,0,1]
	v_fma_f32 v1, v4, v9, v1
	v_mov_b32_e32 v21, v193
	v_pk_mul_f32 v[14:15], v[48:49], v[50:51] op_sel_hi:[1,0]
	v_cvt_pk_fp8_f32 v21, v0, v1
	v_pk_fma_f32 v[10:11], v[10:11], v[14:15], v[18:19]
	v_add_f32_e32 v4, 1.0, v6
	v_fma_f32 v44, v126, v92, v44
	v_fmac_f32_e32 v45, v127, v93
	v_fma_f32 v2, v4, v10, v2
	v_add_f32_e32 v4, 1.0, v7
	v_cvt_pk_fp8_f32 v90, v44, v45 op_sel:[0,0,1]
	v_fmac_f32_e32 v3, v4, v11
	v_cvt_pk_fp8_f32 v21, v2, v3 op_sel:[0,0,1]
	v_lshl_add_u64 v[0:1], s[38:39], 0, v[60:61]
	v_add_co_u32_e32 v0, vcc, s0, v0
	v_lshl_add_u64 v[60:61], v[60:61], 0, s[10:11]
	s_nop 0
	v_addc_co_u32_e32 v1, vcc, 0, v1, vcc
	v_cvt_pk_bf16_f32 v25, v92, v93
	v_cvt_pk_bf16_f32 v26, v30, v31
	v_cvt_pk_bf16_f32 v13, v28, v29
	v_cvt_pk_bf16_f32 v14, v8, v9
	v_cvt_pk_bf16_f32 v15, v10, v11
	global_store_dwordx2 v[0:1], v[90:91], off nt
	global_store_dwordx2 v[0:1], v[20:21], off offset:128 nt
	global_store_dwordx4 v[68:69], v[24:27], off nt
	global_store_dwordx4 v[68:69], v[12:15], off offset:256 nt
	s_cbranch_scc1 .LBB0_775
